# speedup vs baseline: 1.0038x; 1.0038x over previous
.LBB2_9:
	v_subrev_u32_e32 v10, s24, v79
	s_cmp_lg_u32 s24, 0
	v_cmp_lt_i32_e32 vcc, v62, v10
	s_cselect_b64 s[20:21], -1, 0
	s_cbranch_scc1 .Lmy_fullwait
	s_cmp_eq_u32 s15, s2
	s_cbranch_scc1 .Lmy_fullwait
	s_waitcnt vmcnt(1)
	v_mov_b64_e32 v[12:13], v[8:9]
	v_mov_b64_e32 v[10:11], v[6:7]
	v_mov_b32_e32 v17, v64
	s_branch .Lmy_13b
.Lmy_fullwait:
	s_cmp_eq_u32 s24, 0
	s_waitcnt vmcnt(0)
	v_mov_b64_e32 v[12:13], v[8:9]
	v_mov_b64_e32 v[10:11], v[6:7]
	v_mov_b32_e32 v17, v64
	s_cbranch_scc1 .LBB2_13
	v_mov_b32_e32 v10, v91
	v_mov_b32_e32 v17, v86
	s_and_saveexec_b64 s[6:7], vcc
	s_cbranch_execz .LBB2_12
	v_add_lshl_u32 v10, s24, v93, 2
	global_load_dword v17, v10, s[28:29]
	s_waitcnt vmcnt(0)
	v_lshlrev_b32_e32 v10, 5, v17

.Lmy_13b:
	v_pk_add_f32 v[10:11], v[10:11], v[2:3]
	s_nop 0
	v_mul_f32_e32 v55, 0x3e4ccccd, v10
	v_max_f32 v55, v10, v55
	v_mul_f32_e32 v10, 0x3e4ccccd, v11
	v_max_f32 v57, v11, v10
	v_pk_add_f32 v[10:11], v[12:13], v[4:5]
	v_cndmask_b32_e32 v56, v67, v55, vcc
	v_mul_f32_e32 v12, 0x3e4ccccd, v10
	v_mul_f32_e32 v13, 0x3e4ccccd, v11
	v_cndmask_b32_e32 v58, v67, v57, vcc
	v_max_f32 v10, v10, v12
	v_max_f32 v11, v11, v13
	s_nop 0
	v_cndmask_b32_e32 v12, v67, v10, vcc
	v_cndmask_b32_e32 v13, v67, v11, vcc
	s_nop 1
	v_max_f32_dpp v56, v56, v56 quad_perm:[1,0,3,2] row_mask:0xf bank_mask:0xf bound_ctrl:1
	v_max_f32_dpp v58, v58, v58 quad_perm:[1,0,3,2] row_mask:0xf bank_mask:0xf bound_ctrl:1
	v_max_f32_dpp v12, v12, v12 quad_perm:[1,0,3,2] row_mask:0xf bank_mask:0xf bound_ctrl:1
	v_max_f32_dpp v13, v13, v13 quad_perm:[1,0,3,2] row_mask:0xf bank_mask:0xf bound_ctrl:1
	v_max_f32_dpp v56, v56, v56 quad_perm:[2,3,0,1] row_mask:0xf bank_mask:0xf bound_ctrl:1
	v_max_f32_dpp v58, v58, v58 quad_perm:[2,3,0,1] row_mask:0xf bank_mask:0xf bound_ctrl:1
	v_max_f32_dpp v12, v12, v12 quad_perm:[2,3,0,1] row_mask:0xf bank_mask:0xf bound_ctrl:1
	v_max_f32_dpp v13, v13, v13 quad_perm:[2,3,0,1] row_mask:0xf bank_mask:0xf bound_ctrl:1
	v_max_f32_dpp v56, v56, v56 row_half_mirror row_mask:0xf bank_mask:0xf bound_ctrl:1
	v_max_f32_dpp v58, v58, v58 row_half_mirror row_mask:0xf bank_mask:0xf bound_ctrl:1
	v_max_f32_dpp v12, v12, v12 row_half_mirror row_mask:0xf bank_mask:0xf bound_ctrl:1
	v_max_f32_dpp v13, v13, v13 row_half_mirror row_mask:0xf bank_mask:0xf bound_ctrl:1
	v_max_f32_dpp v56, v56, v56 row_mirror row_mask:0xf bank_mask:0xf bound_ctrl:1
	v_max_f32_dpp v58, v58, v58 row_mirror row_mask:0xf bank_mask:0xf bound_ctrl:1
	v_max_f32_dpp v12, v12, v12 row_mirror row_mask:0xf bank_mask:0xf bound_ctrl:1
	v_max_f32_dpp v13, v13, v13 row_mirror row_mask:0xf bank_mask:0xf bound_ctrl:1
	s_nop 0
	s_nop 0
	v_max_f32 v110, v54, v56
	v_max_f32 v112, v15, v12
	v_max_f32 v111, v16, v58
	v_max_f32 v113, v14, v13
	s_nop 0
	v_sub_f32_e32 v54, v54, v110
	v_sub_f32_e32 v10, v10, v112
	v_exp_f32_e32 v114, v54
	v_sub_f32_e32 v54, v55, v110
	v_sub_f32_e32 v55, v57, v111
	v_exp_f32_e32 v12, v10
	v_sub_f32_e32 v10, v11, v113
	v_exp_f32_e32 v54, v54
	v_exp_f32_e32 v55, v55
	v_exp_f32_e32 v13, v10
	v_cndmask_b32_e32 v12, 0, v12, vcc
	v_cndmask_b32_e32 v10, 0, v54, vcc
	v_cndmask_b32_e32 v11, 0, v55, vcc
	v_cndmask_b32_e32 v13, 0, v13, vcc
	v_cndmask_b32_e64 v54, 0, 1, s[20:21]
	v_mov_b32_e32 v83, v12
	v_mov_b32_e32 v102, v11
	v_mov_b32_e32 v80, v13
	v_mov_b32_e32 v106, v10
	v_cmp_ne_u32_e64 s[6:7], 1, v54
	s_andn2_b64 vcc, exec, s[20:21]
	s_nop 1
	v_add_f32_dpp v106, v106, v106 quad_perm:[1,0,3,2] row_mask:0xf bank_mask:0xf bound_ctrl:1
	v_add_f32_dpp v102, v102, v102 quad_perm:[1,0,3,2] row_mask:0xf bank_mask:0xf bound_ctrl:1
	v_add_f32_dpp v83, v83, v83 quad_perm:[1,0,3,2] row_mask:0xf bank_mask:0xf bound_ctrl:1
	v_add_f32_dpp v80, v80, v80 quad_perm:[1,0,3,2] row_mask:0xf bank_mask:0xf bound_ctrl:1
	v_add_f32_dpp v106, v106, v106 quad_perm:[2,3,0,1] row_mask:0xf bank_mask:0xf bound_ctrl:1
	v_add_f32_dpp v102, v102, v102 quad_perm:[2,3,0,1] row_mask:0xf bank_mask:0xf bound_ctrl:1
	v_add_f32_dpp v83, v83, v83 quad_perm:[2,3,0,1] row_mask:0xf bank_mask:0xf bound_ctrl:1
	v_add_f32_dpp v80, v80, v80 quad_perm:[2,3,0,1] row_mask:0xf bank_mask:0xf bound_ctrl:1
	v_add_f32_dpp v106, v106, v106 row_half_mirror row_mask:0xf bank_mask:0xf bound_ctrl:1
	v_add_f32_dpp v102, v102, v102 row_half_mirror row_mask:0xf bank_mask:0xf bound_ctrl:1
	v_add_f32_dpp v83, v83, v83 row_half_mirror row_mask:0xf bank_mask:0xf bound_ctrl:1
	v_add_f32_dpp v80, v80, v80 row_half_mirror row_mask:0xf bank_mask:0xf bound_ctrl:1
	v_add_f32_dpp v106, v106, v106 row_mirror row_mask:0xf bank_mask:0xf bound_ctrl:1
	v_add_f32_dpp v102, v102, v102 row_mirror row_mask:0xf bank_mask:0xf bound_ctrl:1
	v_add_f32_dpp v83, v83, v83 row_mirror row_mask:0xf bank_mask:0xf bound_ctrl:1
	v_add_f32_dpp v80, v80, v80 row_mirror row_mask:0xf bank_mask:0xf bound_ctrl:1
	s_nop 0
	s_cbranch_vccnz .LBB2_15
	v_cvt_f16_f32_e32 v54, v114
	v_pk_mul_f16 v109, v54, v109 op_sel_hi:[0,1]
	v_pk_mul_f16 v108, v54, v108 op_sel_hi:[0,1]
	v_pk_mul_f16 v107, v54, v107 op_sel_hi:[0,1]
	v_pk_mul_f16 v105, v54, v105 op_sel_hi:[0,1]
